# HGRN step C (Lever 8): the QE*S MFMAs' LDS operand reads are issued four MFMAs ahead into free registers instead of read-wait-MFMA one at a time (14 of 16 MFMAs)
# baseline (speedup 1.0000x reference)
.LBB0_666:
	ds_read_b64_tr_b16 v[78:79], v157 offset:53248
	ds_read_b64_tr_b16 v[80:81], v157 offset:54400
	ds_read_b64_tr_b16 v[74:75], v157 offset:62464
	ds_read_b64_tr_b16 v[76:77], v157 offset:63616
	ds_read_b128 v[82:85], v158
	ds_read_b128 v[86:89], v158 offset:2304
	ds_read_b128 v[90:93], v158 offset:4608
	ds_read_b128 v[94:97], v158 offset:4672
	ds_read_b128 v[98:101], v158 offset:6976
	v_add_u32_e32 v108, v137, v135
	v_add_u32_e32 v104, v137, v141
	s_waitcnt lgkmcnt(4)
	v_mfma_f32_16x16x32_bf16 v[82:85], v[82:85], v[78:81], 0
	v_add_u32_e32 v122, v142, v135
	v_add_u32_e32 v123, v143, v135
	v_add_u32_e32 v171, v144, v135
	s_waitcnt lgkmcnt(2)
	v_mfma_f32_16x16x32_bf16 v[90:93], v[90:93], v[78:81], 0
	s_lshl_b32 s30, s49, 6
	s_add_i32 s49, s49, 1
	s_add_u32 s38, s38, 0x240000
	s_waitcnt lgkmcnt(1)
	v_mfma_f32_16x16x32_bf16 v[90:93], v[94:97], v[74:77], v[90:93]
	ds_read_b128 v[94:97], v158 offset:6912
	s_addc_u32 s39, s39, 0
	s_mov_b64 s[26:27], 0x20000
	v_mfma_f32_16x16x32_bf16 v[86:89], v[86:89], v[78:81], 0
	v_lshl_add_u64 v[120:121], v[120:121], 0, s[26:27]
	s_cmp_lg_u32 s38, 0x4800000
	s_waitcnt lgkmcnt(0)
	v_mfma_f32_16x16x32_bf16 v[94:97], v[94:97], v[78:81], 0
	v_mfma_f32_16x16x32_bf16 v[94:97], v[98:101], v[74:77], v[94:97]
	ds_read_b64 v[210:211], v108
	ds_read_b64 v[212:213], v104
	ds_read_b64 v[214:215], v122
	v_add_u32_e32 v227, v141, v142
	ds_read_b64 v[216:217], v227
	ds_read_b64 v[218:219], v123
	v_add_u32_e32 v227, v141, v143
	ds_read_b64 v[220:221], v227
	ds_read_b64 v[222:223], v171
	v_add_u32_e32 v227, v141, v144
	ds_read_b64 v[224:225], v227
	v_cvt_pk_bf16_f32 v98, v26, v27
	v_cvt_pk_bf16_f32 v99, v28, v29
	v_cvt_pk_bf16_f32 v100, v30, v31
	v_cvt_pk_bf16_f32 v101, v32, v33
	s_nop 1
	s_waitcnt lgkmcnt(6)
	v_mfma_f32_16x16x32_bf16 v[82:85], v[210:213], v[98:101], v[82:85]
	v_add_u32_e32 v226, v137, v145
	ds_read_b64 v[210:211], v226
	v_add_u32_e32 v227, v137, v146
	ds_read_b64 v[212:213], v227
	s_waitcnt lgkmcnt(6)
	v_mfma_f32_16x16x32_bf16 v[86:89], v[214:217], v[98:101], v[86:89]
	v_add_u32_e32 v226, v142, v145
	ds_read_b64 v[214:215], v226
	v_add_u32_e32 v227, v142, v146
	ds_read_b64 v[216:217], v227
	s_waitcnt lgkmcnt(6)
	v_mfma_f32_16x16x32_bf16 v[90:93], v[218:221], v[98:101], v[90:93]
	v_add_u32_e32 v226, v143, v145
	ds_read_b64 v[218:219], v226
	v_add_u32_e32 v227, v143, v146
	ds_read_b64 v[220:221], v227
	s_waitcnt lgkmcnt(6)
	v_mfma_f32_16x16x32_bf16 v[94:97], v[222:225], v[98:101], v[94:97]
	v_add_u32_e32 v226, v144, v145
	ds_read_b64 v[222:223], v226
	v_add_u32_e32 v227, v144, v146
	ds_read_b64 v[224:225], v227
	v_cvt_pk_bf16_f32 v98, v62, v63
	v_cvt_pk_bf16_f32 v99, v64, v65
	v_cvt_pk_bf16_f32 v100, v54, v55
	v_cvt_pk_bf16_f32 v101, v56, v57
	s_nop 1
	s_waitcnt lgkmcnt(6)
	v_mfma_f32_16x16x32_bf16 v[82:85], v[210:213], v[98:101], v[82:85]
	ds_read2_b64 v[210:213], v108 offset0:16 offset1:20
	s_waitcnt lgkmcnt(5)
	v_mfma_f32_16x16x32_bf16 v[86:89], v[214:217], v[98:101], v[86:89]
	ds_read2_b64 v[214:217], v122 offset0:16 offset1:20
	s_waitcnt lgkmcnt(4)
	v_mfma_f32_16x16x32_bf16 v[90:93], v[218:221], v[98:101], v[90:93]
	ds_read2_b64 v[218:221], v123 offset0:16 offset1:20
	s_waitcnt lgkmcnt(3)
	v_mfma_f32_16x16x32_bf16 v[94:97], v[222:225], v[98:101], v[94:97]
	ds_read2_b64 v[222:225], v171 offset0:16 offset1:20
	v_cvt_pk_bf16_f32 v98, v34, v35
	v_cvt_pk_bf16_f32 v99, v36, v37
	v_cvt_pk_bf16_f32 v100, v50, v51
	v_cvt_pk_bf16_f32 v101, v52, v53
	s_nop 1
	s_waitcnt lgkmcnt(3)
	v_mfma_f32_16x16x32_bf16 v[82:85], v[210:213], v[98:101], v[82:85]
	ds_read2_b64 v[210:213], v108 offset0:24 offset1:28
	s_waitcnt lgkmcnt(3)
	v_mfma_f32_16x16x32_bf16 v[86:89], v[214:217], v[98:101], v[86:89]
	ds_read2_b64 v[214:217], v122 offset0:24 offset1:28
	s_waitcnt lgkmcnt(3)
	v_mfma_f32_16x16x32_bf16 v[90:93], v[218:221], v[98:101], v[90:93]
	s_waitcnt lgkmcnt(2)
	v_mfma_f32_16x16x32_bf16 v[94:97], v[222:225], v[98:101], v[94:97]
	v_cvt_pk_bf16_f32 v98, v42, v43
	v_cvt_pk_bf16_f32 v99, v44, v45
	v_cvt_pk_bf16_f32 v100, v58, v59
	v_cvt_pk_bf16_f32 v101, v60, v61
	s_nop 1
	s_waitcnt lgkmcnt(1)
	v_mfma_f32_16x16x32_bf16 v[82:85], v[210:213], v[98:101], v[82:85]
	s_waitcnt lgkmcnt(0)
	v_mfma_f32_16x16x32_bf16 v[86:89], v[214:217], v[98:101], v[86:89]
	ds_read2_b64 v[102:105], v123 offset0:24 offset1:28
	v_lshl_add_u64 v[122:123], v[118:119], 0, s[30:31]
	s_waitcnt lgkmcnt(0)
	v_mfma_f32_16x16x32_bf16 v[90:93], v[102:105], v[98:101], v[90:93]
	ds_read2_b64 v[102:105], v171 offset0:24 offset1:28
	ds_write2_b32 v159, v82, v83 offset1:132
	v_add_u32_e32 v82, 0x400, v159
	s_waitcnt lgkmcnt(1)
	v_mfma_f32_16x16x32_bf16 v[94:97], v[102:105], v[98:101], v[94:97]
	ds_write2_b32 v82, v84, v85 offset0:8 offset1:140
	ds_write_b32 v160, v86
	v_add_u32_e32 v82, 0x2200, v159
	ds_write2_b32 v82, v87, v88 offset0:68 offset1:200
	ds_write_b32 v159, v89 offset:10032
	ds_write_b32 v160, v90 offset:8448
	v_add_u32_e32 v82, 0x4400, v159
	ds_write2_b32 v82, v91, v92 offset0:4 offset1:136
	ds_write_b32 v159, v93 offset:18480
	ds_write_b32 v160, v94 offset:16896
	v_add_u32_e32 v82, 0x6400, v159
	ds_write2_b32 v82, v95, v96 offset0:68 offset1:200
	ds_write_b32 v159, v97 offset:26928
	v_add_u32_e32 v92, 0x1c000, v134
	ds_read_b128 v[82:85], v92
	s_waitcnt lgkmcnt(0)
	v_pk_mul_f32 v[26:27], v[26:27], v[82:83]
	v_add_u32_e32 v82, v140, v136
	v_pk_mul_f32 v[28:29], v[28:29], v[84:85]
	ds_read_b64_tr_b16 v[86:87], v82 offset:35968
	ds_read_b64_tr_b16 v[84:85], v82 offset:34816
	ds_read_b64_tr_b16 v[88:89], v82 offset:34848
	s_waitcnt lgkmcnt(1)
	v_mfma_f32_16x16x32_bf16 v[26:29], v[84:87], v[78:81], v[26:29]
	ds_read_b64_tr_b16 v[84:85], v82 offset:44032
	ds_read_b64_tr_b16 v[86:87], v82 offset:45184
	ds_read_b64_tr_b16 v[90:91], v82 offset:36000
	s_waitcnt lgkmcnt(1)
	v_mfma_f32_16x16x32_bf16 v[26:29], v[84:87], v[74:77], v[26:29]
	ds_read_b128 v[84:87], v92 offset:64
	s_waitcnt lgkmcnt(0)
	v_pk_mul_f32 v[30:31], v[30:31], v[84:85]
	v_pk_mul_f32 v[32:33], v[32:33], v[86:87]
	ds_read_b64_tr_b16 v[84:85], v82 offset:44064
	ds_read_b64_tr_b16 v[86:87], v82 offset:45216
	v_mfma_f32_16x16x32_bf16 v[30:33], v[88:91], v[78:81], v[30:33]
	s_waitcnt lgkmcnt(0)
	v_mfma_f32_16x16x32_bf16 v[30:33], v[84:87], v[74:77], v[30:33]
	ds_read_b128 v[84:87], v92 offset:128
	s_waitcnt lgkmcnt(0)
	v_pk_mul_f32 v[62:63], v[62:63], v[84:85]
	v_pk_mul_f32 v[64:65], v[64:65], v[86:87]
	ds_read_b64_tr_b16 v[84:85], v82 offset:34880
	ds_read_b64_tr_b16 v[86:87], v82 offset:36032
	s_waitcnt lgkmcnt(0)
	v_mfma_f32_16x16x32_bf16 v[62:65], v[84:87], v[78:81], v[62:65]
	ds_read_b64_tr_b16 v[84:85], v82 offset:44096
	ds_read_b64_tr_b16 v[86:87], v82 offset:45248
	s_waitcnt lgkmcnt(0)
	v_mfma_f32_16x16x32_bf16 v[62:65], v[84:87], v[74:77], v[62:65]
	ds_read_b128 v[84:87], v92 offset:192
	s_waitcnt lgkmcnt(0)
	v_pk_mul_f32 v[54:55], v[54:55], v[84:85]
	v_pk_mul_f32 v[56:57], v[56:57], v[86:87]
	ds_read_b64_tr_b16 v[84:85], v82 offset:34912
	ds_read_b64_tr_b16 v[86:87], v82 offset:36064
	s_waitcnt lgkmcnt(0)
	v_mfma_f32_16x16x32_bf16 v[54:57], v[84:87], v[78:81], v[54:57]
	ds_read_b64_tr_b16 v[84:85], v82 offset:44128
	ds_read_b64_tr_b16 v[86:87], v82 offset:45280
	s_waitcnt lgkmcnt(0)
	v_mfma_f32_16x16x32_bf16 v[54:57], v[84:87], v[74:77], v[54:57]
	ds_read_b128 v[84:87], v92 offset:256
	s_waitcnt lgkmcnt(0)
	v_pk_mul_f32 v[34:35], v[34:35], v[84:85]
	v_pk_mul_f32 v[36:37], v[36:37], v[86:87]
	ds_read_b64_tr_b16 v[84:85], v82 offset:34944
	ds_read_b64_tr_b16 v[86:87], v82 offset:36096
	s_waitcnt lgkmcnt(0)
	v_mfma_f32_16x16x32_bf16 v[34:37], v[84:87], v[78:81], v[34:37]
	ds_read_b64_tr_b16 v[84:85], v82 offset:44160
	ds_read_b64_tr_b16 v[86:87], v82 offset:45312
	s_waitcnt lgkmcnt(0)
	v_mfma_f32_16x16x32_bf16 v[34:37], v[84:87], v[74:77], v[34:37]
	ds_read_b128 v[84:87], v92 offset:320
	s_waitcnt lgkmcnt(0)
	v_pk_mul_f32 v[50:51], v[50:51], v[84:85]
	v_pk_mul_f32 v[52:53], v[52:53], v[86:87]
	ds_read_b64_tr_b16 v[84:85], v82 offset:34976
	ds_read_b64_tr_b16 v[86:87], v82 offset:36128
	s_waitcnt lgkmcnt(0)
	v_mfma_f32_16x16x32_bf16 v[50:53], v[84:87], v[78:81], v[50:53]
	ds_read_b64_tr_b16 v[84:85], v82 offset:44192
	ds_read_b64_tr_b16 v[86:87], v82 offset:45344
	s_waitcnt lgkmcnt(0)
	v_mfma_f32_16x16x32_bf16 v[50:53], v[84:87], v[74:77], v[50:53]
	ds_read_b128 v[84:87], v92 offset:384
	s_waitcnt lgkmcnt(0)
	v_pk_mul_f32 v[42:43], v[42:43], v[84:85]
	v_pk_mul_f32 v[44:45], v[44:45], v[86:87]
	ds_read_b64_tr_b16 v[84:85], v82 offset:35008
	ds_read_b64_tr_b16 v[86:87], v82 offset:36160
	s_waitcnt lgkmcnt(0)
	v_mfma_f32_16x16x32_bf16 v[42:45], v[84:87], v[78:81], v[42:45]
	ds_read_b64_tr_b16 v[84:85], v82 offset:44224
	ds_read_b64_tr_b16 v[86:87], v82 offset:45376
	s_waitcnt lgkmcnt(0)
	v_mfma_f32_16x16x32_bf16 v[42:45], v[84:87], v[74:77], v[42:45]
	ds_read_b128 v[84:87], v92 offset:448
	s_waitcnt lgkmcnt(0)
	v_pk_mul_f32 v[58:59], v[58:59], v[84:85]
	v_pk_mul_f32 v[60:61], v[60:61], v[86:87]
	ds_read_b64_tr_b16 v[84:85], v82 offset:35040
	ds_read_b64_tr_b16 v[86:87], v82 offset:36192
	s_waitcnt lgkmcnt(0)
	v_mfma_f32_16x16x32_bf16 v[58:61], v[84:87], v[78:81], v[58:61]
	ds_read_b64_tr_b16 v[78:79], v82 offset:44256
	ds_read_b64_tr_b16 v[80:81], v82 offset:45408
	s_waitcnt lgkmcnt(0)
	s_barrier
	s_waitcnt lgkmcnt(0)
	v_mfma_f32_16x16x32_bf16 v[58:61], v[78:81], v[74:77], v[58:61]
	ds_read_b128 v[86:89], v161
	ds_read_b128 v[82:85], v161 offset:16
	ds_read_b128 v[78:81], v161 offset:32
	ds_read_b128 v[74:77], v161 offset:48
	s_waitcnt lgkmcnt(3)
	v_pk_mul_f32 v[90:91], v[88:89], v[88:89]
	v_pk_mul_f32 v[92:93], v[86:87], v[86:87]
	s_nop 0
	v_pk_mov_b32 v[94:95], v[92:93], v[90:91] op_sel:[1,0]
	v_mov_b32_e32 v93, v91
	v_pk_add_f32 v[90:91], v[94:95], v[92:93]
	s_waitcnt lgkmcnt(2)
	v_pk_mul_f32 v[92:93], v[84:85], v[84:85]
	v_pk_mul_f32 v[94:95], v[82:83], v[82:83]
	v_pk_add_f32 v[90:91], v[90:91], v[90:91] op_sel:[0,1] op_sel_hi:[1,0]
	v_pk_mov_b32 v[96:97], v[94:95], v[92:93] op_sel:[1,0]
	v_mov_b32_e32 v95, v93
	v_pk_add_f32 v[92:93], v[96:97], v[94:95]
	s_waitcnt lgkmcnt(0)
	v_mul_f32_e32 v94, v74, v74
	v_mul_f32_e32 v95, v75, v75
	v_pk_add_f32 v[92:93], v[92:93], v[92:93] op_sel:[0,1] op_sel_hi:[1,0]
	v_mov_b32_e32 v91, v94
	v_mov_b32_e32 v93, v95
	v_pk_add_f32 v[90:91], v[90:91], v[92:93]
	v_mul_f32_e32 v92, v79, v79
	v_mul_f32_e32 v94, v81, v81
	v_mul_f32_e32 v96, v76, v76
	v_mul_f32_e32 v97, v77, v77
	v_pk_fma_f32 v[92:93], v[78:79], v[78:79], v[92:93] op_sel_hi:[1,1,0]
	v_pk_fma_f32 v[94:95], v[80:81], v[80:81], v[94:95] op_sel_hi:[1,1,0]
	v_mov_b32_e32 v93, v96
	v_mov_b32_e32 v95, v97
	v_pk_add_f32 v[92:93], v[92:93], v[94:95]
	s_nop 0
	v_pk_add_f32 v[90:91], v[90:91], v[92:93]
	v_and_b32_e32 v92, 64, v166
	v_add_f32_e32 v90, v90, v91
	v_xor_b32_e32 v91, 1, v166
	v_add_u32_e32 v92, 64, v92
	v_cmp_lt_i32_e32 vcc, v91, v92
	s_nop 1
	v_cndmask_b32_e32 v91, v166, v91, vcc
	v_lshlrev_b32_e32 v91, 2, v91
	ds_bpermute_b32 v91, v91, v90
	s_waitcnt lgkmcnt(0)
	v_add_f32_e32 v90, v90, v91
	v_xor_b32_e32 v91, 2, v166
	v_cmp_lt_i32_e32 vcc, v91, v92
	s_nop 1
	v_cndmask_b32_e32 v91, v166, v91, vcc
	v_lshlrev_b32_e32 v91, 2, v91
	ds_bpermute_b32 v91, v91, v90
	s_waitcnt lgkmcnt(0)
	v_add_f32_e32 v90, v90, v91
	v_xor_b32_e32 v91, 4, v166
	v_cmp_lt_i32_e32 vcc, v91, v92
	s_nop 1
	v_cndmask_b32_e32 v91, v166, v91, vcc
	v_lshlrev_b32_e32 v91, 2, v91
	ds_bpermute_b32 v91, v91, v90
	s_waitcnt lgkmcnt(0)
	v_add_f32_e32 v90, v90, v91
	v_fmamk_f32 v90, v90, 0x3c000000, v162
	v_cmp_gt_f32_e32 vcc, s45, v90
	v_mul_f32_e32 v91, 0x4b800000, v90
	s_nop 0
	v_cndmask_b32_e32 v90, v90, v91, vcc
	v_rsq_f32_e32 v90, v90
	s_nop 0
	v_mul_f32_e32 v91, 0x45800000, v90
	v_cndmask_b32_e32 v108, v90, v91, vcc
	v_mov_b64_e32 v[90:91], v[194:195]
	v_mov_b64_e32 v[92:93], v[196:197]
	v_mov_b64_e32 v[94:95], v[198:199]
	v_mov_b64_e32 v[96:97], v[200:201]
	v_mov_b64_e32 v[98:99], v[202:203]
	v_mov_b64_e32 v[100:101], v[204:205]
	v_mov_b64_e32 v[102:103], v[206:207]
	v_mov_b64_e32 v[104:105], v[208:209]
	v_mul_f32_e32 v86, v86, v108
	v_mul_f32_e32 v87, v87, v108
	v_mul_f32_e32 v83, v83, v108
	v_mul_f32_e32 v79, v79, v108
	v_mul_f32_e32 v74, v74, v108
	v_mul_f32_e32 v82, v82, v108
	v_mul_f32_e32 v78, v78, v108
	v_mul_f32_e32 v74, v90, v74
	v_mul_f32_e32 v79, v95, v79
	v_mul_f32_e32 v83, v99, v83
	v_mul_f32_e32 v86, v102, v86
	v_lshlrev_b32_e32 v102, 16, v46
	v_mul_f32_e32 v87, v103, v87
	v_and_b32_e32 v46, 0xffff0000, v46
	v_mul_f32_e32 v46, v87, v46
	v_mul_f32_e32 v87, v88, v108
	v_mul_f32_e32 v87, v104, v87
	v_lshlrev_b32_e32 v88, 16, v47
	v_mul_f32_e32 v87, v87, v88
	v_mul_f32_e32 v88, v89, v108
	v_mul_f32_e32 v88, v105, v88
	v_and_b32_e32 v47, 0xffff0000, v47
	v_mul_f32_e32 v47, v88, v47
	v_lshlrev_b32_e32 v88, 16, v48
	v_and_b32_e32 v48, 0xffff0000, v48
	v_mul_f32_e32 v48, v83, v48
	v_mul_f32_e32 v83, v84, v108
	v_mul_f32_e32 v83, v100, v83
	v_lshlrev_b32_e32 v84, 16, v49
	v_mul_f32_e32 v83, v83, v84
	v_mul_f32_e32 v84, v85, v108
	v_mul_f32_e32 v84, v101, v84
	v_and_b32_e32 v49, 0xffff0000, v49
	v_mul_f32_e32 v49, v84, v49
	v_lshlrev_b32_e32 v84, 16, v38
	v_and_b32_e32 v38, 0xffff0000, v38
	v_mul_f32_e32 v38, v79, v38
	v_mul_f32_e32 v79, v80, v108
	v_mul_f32_e32 v79, v96, v79
	v_lshlrev_b32_e32 v80, 16, v39
	v_mul_f32_e32 v79, v79, v80
	v_mul_f32_e32 v80, v81, v108
	v_mul_f32_e32 v80, v97, v80
	v_and_b32_e32 v39, 0xffff0000, v39
	v_mul_f32_e32 v39, v80, v39
	v_lshlrev_b32_e32 v80, 16, v40
	v_mul_f32_e32 v80, v74, v80
	v_mul_f32_e32 v74, v75, v108
	v_mul_f32_e32 v74, v91, v74
	v_and_b32_e32 v40, 0xffff0000, v40
	v_mul_f32_e32 v40, v74, v40
	v_mul_f32_e32 v74, v76, v108
	v_mul_f32_e32 v74, v92, v74
	v_lshlrev_b32_e32 v75, 16, v41
	v_mul_f32_e32 v81, v74, v75
	v_mul_f32_e32 v74, v77, v108
	v_mul_f32_e32 v82, v98, v82
	v_mul_f32_e32 v78, v94, v78
	v_mul_f32_e32 v74, v93, v74
	v_and_b32_e32 v41, 0xffff0000, v41
	v_mul_f32_e32 v86, v86, v102
	v_mul_f32_e32 v82, v82, v88
	v_mul_f32_e32 v78, v78, v84
	v_mul_f32_e32 v41, v74, v41
	v_mov_b32_e32 v74, 0
	v_mov_b32_e32 v75, 0
	v_mov_b32_e32 v76, 0
	v_mov_b32_e32 v77, 0
	v_cvt_pk_fp8_f32 v74, v86, v46
	v_cvt_pk_fp8_f32 v75, v82, v48
	v_cvt_pk_fp8_f32 v76, v78, v38
	v_cvt_pk_fp8_f32 v77, v80, v40
	v_cvt_pk_fp8_f32 v74, v87, v47 op_sel:[0,0,1]
	v_cvt_pk_fp8_f32 v75, v83, v49 op_sel:[0,0,1]
	v_cvt_pk_fp8_f32 v76, v79, v39 op_sel:[0,0,1]
	v_cvt_pk_fp8_f32 v77, v81, v41 op_sel:[0,0,1]
	v_lshlrev_b64 v[38:39], 11, v[122:123]
	v_lshl_add_u64 v[78:79], v[116:117], 0, v[38:39]
	s_cbranch_scc0 .LBB0_642
	s_waitcnt vmcnt(0)
	v_mov_b64_e32 v[38:39], v[70:71]
	v_mov_b64_e32 v[46:47], v[66:67]
	v_mov_b64_e32 v[40:41], v[72:73]
	v_mov_b64_e32 v[48:49], v[68:69]
	s_branch .LBB0_650
